# speedup vs baseline: 1.0216x; 1.0054x over previous
.Lno_warm:
	v_mfma_f32_16x16x32_f16 v[14:17], a[92:95], v[252:255], v[14:17]
	v_mfma_f32_16x16x32_f16 v[18:21], a[120:123], v[248:251], v[18:21]
	v_mfma_f32_16x16x32_f16 v[18:21], a[124:127], v[252:255], v[18:21]
	v_mfma_f32_16x16x32_f16 v[22:25], a[152:155], v[248:251], v[22:25]
	v_mfma_f32_16x16x32_f16 v[22:25], a[156:159], v[252:255], v[22:25]
	s_mov_b64 exec, s[2:3]
	ds_write_b128 v174, v[6:9]
	v_mfma_f32_16x16x32_f16 v[26:29], a[184:187], v[248:251], v[26:29]
	v_mfma_f32_16x16x32_f16 v[26:29], a[188:191], v[252:255], v[26:29]
	ds_write_b128 v174, v[10:13] offset:512
	v_mfma_f32_16x16x32_f16 v[30:33], a[216:219], v[248:251], v[30:33]
	v_mfma_f32_16x16x32_f16 v[30:33], a[220:223], v[252:255], v[30:33]
	ds_write_b128 v174, v[14:17] offset:1024
	v_mfma_f32_16x16x32_f16 v[34:37], a[248:251], v[248:251], v[34:37]
	v_mfma_f32_16x16x32_f16 v[34:37], a[252:255], v[252:255], v[34:37]
	ds_write_b128 v174, v[18:21] offset:1536
	ds_write_b128 v174, v[22:25] offset:2048
	ds_write_b128 v174, v[26:29] offset:2560
	v_mov_b64_e32 v[6:7], 0
	v_mov_b64_e32 v[8:9], 0
	ds_write_b128 v174, v[30:33] offset:3072
	v_mov_b64_e32 v[10:11], 0
	v_mov_b64_e32 v[12:13], 0
	ds_write_b128 v174, v[34:37] offset:3584
	s_branch .Lwrites_done
.Lall_chunks_done:
	s_and_saveexec_b64 s[12:13], s[2:3]
	ds_write_b128 v174, v[6:9]
	ds_write_b128 v174, v[10:13] offset:512
	ds_write_b128 v174, v[14:17] offset:1024
	ds_write_b128 v174, v[18:21] offset:1536
	ds_write_b128 v174, v[22:25] offset:2048
	ds_write_b128 v174, v[26:29] offset:2560
	ds_write_b128 v174, v[30:33] offset:3072
	ds_write_b128 v174, v[34:37] offset:3584
	v_mov_b64_e32 v[6:7], 0
	v_mov_b64_e32 v[8:9], 0
	v_mov_b64_e32 v[10:11], 0
	v_mov_b64_e32 v[12:13], 0
.Lwrites_done:
	s_mov_b64 exec, -1
	s_waitcnt lgkmcnt(0)
	s_barrier
	ds_read_b128 v[2:5], v175
	ds_read_b128 v[224:227], v175 offset:4096
	ds_read_b128 v[228:231], v175 offset:8192
	ds_read_b128 v[232:235], v175 offset:12288
	s_mov_b64 exec, s[2:3]
	v_mov_b64_e32 v[14:15], 0
	v_mov_b64_e32 v[16:17], 0
	v_mov_b64_e32 v[18:19], 0
	v_mov_b64_e32 v[20:21], 0
	v_mov_b64_e32 v[22:23], 0
	v_mov_b64_e32 v[24:25], 0
	v_mov_b64_e32 v[26:27], 0
	v_mov_b64_e32 v[28:29], 0
	v_mov_b64_e32 v[30:31], 0
	v_mov_b64_e32 v[32:33], 0
	v_mov_b64_e32 v[34:35], 0
	v_mov_b64_e32 v[36:37], 0
	s_mov_b64 exec, -1
	s_waitcnt lgkmcnt(0)
	v_pk_add_f32 v[4:5], v[4:5], v[226:227]
	v_pk_add_f32 v[2:3], v[2:3], v[224:225]
	v_pk_add_f32 v[4:5], v[4:5], v[230:231]
	v_pk_add_f32 v[2:3], v[2:3], v[228:229]
	v_pk_add_f32 v[4:5], v[4:5], v[234:235]
	v_pk_add_f32 v[2:3], v[2:3], v[232:233]
	v_fma_f32 v4, v4, s37, v187
	v_fma_f32 v2, v2, s38, v185
	v_exp_f32_e32 v4, v4
	v_fma_f32 v3, v3, s38, v186
	v_exp_f32_e32 v2, v2
	v_fma_f32 v5, v5, s38, v188
	v_exp_f32_e32 v3, v3
	v_add_f32_e32 v4, 1.0, v4
	v_add_f32_e32 v2, 1.0, v2
	v_rcp_f32_e32 v4, v4
	v_rcp_f32_e32 v2, v2
	v_add_f32_e32 v3, 1.0, v3
	v_rcp_f32_e32 v3, v3
	v_exp_f32_e32 v5, v5
	v_fma_f32 v4, v4, -2.0, 1.0
	v_mul_f32_e32 v2, v2, v4
	v_add_f32_e32 v4, 1.0, v5
	v_fmac_f32_e32 v2, v177, v3
	v_rcp_f32_e32 v5, v4
	v_mul_f32_e32 v3, 0x4038aa3b, v2
	v_exp_f32_e32 v3, v3
	v_mov_b32_e32 v177, v2
	v_add_f32_e32 v3, 1.0, v3
	v_rcp_f32_e32 v3, v3
	s_nop 0
	v_fma_f32 v3, v3, -2.0, 1.0
	v_mul_f32_e32 v4, v5, v3
	v_fma_mixlo_f16 v3, v5, v3, 0
	v_and_b32_e32 v3, 0xffffbfff, v3
	v_or_b32_sdwa v108, s34, v3 dst_sel:DWORD dst_unused:UNUSED_PAD src0_sel:DWORD src1_sel:WORD_0
	s_nop 1
	v_mov_b32_dpp v109, v108 row_ror:8 row_mask:0xf bank_mask:0xf
	v_mov_b32_dpp v5, v4 row_ror:8 row_mask:0xf bank_mask:0xf
	s_and_saveexec_b64 s[12:13], s[0:1]
	v_lshl_or_b32 v108, v109, 16, v108
	s_andn2_b64 vcc, exec, s[4:5]
	s_cbranch_vccnz .Lpub_sc1
	buffer_store_dword v108, v176, s[8:11], 0 offen
